# MoE-down GEMM: partial fifth round split between two workgroups by row half (other half's MFMA blocks skipped, its rows marked invalid); row weights now requested for all lanes before the first row
# baseline (speedup 1.0000x reference)
.LBB0_1476:
	v_readlane_b32 s19, v254, 49
	s_add_i32 s49, s1, 1
	v_readlane_b32 s21, v253, 52
	v_mov_b32_e32 v114, s19
	ds_read_b32 v114, v114
	s_mul_i32 s19, s49, s94
	s_add_i32 s19, s21, s19
	s_cmp_eq_u32 s49, 4
	s_cbranch_scc0 .Lt10_map
	s_cmp_eq_u32 s94, 0x100
	s_cbranch_scc0 .Lt10_map
	s_lshr_b32 s19, s21, 1
	s_addk_i32 s19, 0x400
.Lt10_map:
	v_mov_b32_e32 v233, 0x3a800000
	s_waitcnt lgkmcnt(0)
	v_readfirstlane_b32 s21, v114
	s_lshl_b32 s21, s21, 2
	s_cmp_lt_i32 s19, s21
	s_cselect_b64 s[30:31], -1, 0
	s_cmp_ge_i32 s19, s21
	s_cselect_b64 s[24:25], -1, 0
	s_and_b64 vcc, exec, s[24:25]
	s_cbranch_vccnz .LBB0_1478
	s_and_b32 s18, s19, -4
	s_add_i32 s20, 0, 0x20000
	s_add_i32 s18, s20, s18
	v_mov_b32_e32 v114, s18
	ds_read_b32 v114, v114 offset:288
	s_waitcnt lgkmcnt(0)
	v_readfirstlane_b32 s18, v114
	s_lshl_b32 s21, s18, 2
	s_add_i32 s18, s20, s21
	v_mov_b32_e32 v132, s18
	ds_read2_b32 v[132:133], v132 offset1:32
	s_ashr_i32 s18, s19, 2
	s_and_b32 s19, s19, 3
	v_lshlrev_b32_e32 v114, 15, v114
	s_or_b32 s20, s21, s19
	s_waitcnt lgkmcnt(0)
	v_sub_u32_e32 v133, s18, v133
	v_lshlrev_b32_e32 v133, 8, v133
	v_sub_u32_e32 v132, v132, v133
	v_add_u32_e32 v186, v133, v114
	v_min_i32_e32 v185, 0x100, v132
.LBB0_1478:
	s_add_u32 s50, s34, 0x100
	s_addc_u32 s51, s35, 0
	s_ashr_i32 s19, s18, 31
	s_lshl_b64 s[26:27], s[18:19], 18
	v_readlane_b32 s28, v253, 19
	v_readlane_b32 s29, v253, 20
	s_add_u32 s26, s28, s26
	s_addc_u32 s27, s29, s27
	s_and_b64 s[28:29], s[30:31], exec
	s_cselect_b32 s19, s27, s23
	s_cselect_b32 s52, s26, s22
	s_ashr_i32 s21, s20, 31
	s_lshl_b64 s[28:29], s[20:21], 18
	s_add_u32 s28, s2, s28
	s_addc_u32 s29, s3, s29
	s_and_b64 s[38:39], s[30:31], exec
	s_cselect_b32 s21, s29, s35
	s_cselect_b32 s53, s28, s34
	s_add_u32 s34, s22, 0x20080
	s_addc_u32 s35, s23, 0
	v_lshl_add_u64 v[132:133], s[34:35], 0, v[148:149]
	v_lshl_add_u64 v[134:135], s[34:35], 0, v[150:151]
	s_mov_b32 s54, -2
	s_mov_b64 s[34:35], 0
	s_mov_b32 s37, 0
	s_cmp_eq_u32 s49, 5
	s_cbranch_scc0 .Lt10_flag
	s_cmp_eq_u32 s94, 0x100
	s_cbranch_scc0 .Lt10_flag
	v_readlane_b32 s37, v253, 52
	s_and_b32 s37, s37, 1
	s_xor_b32 s37, s37, 1
	s_add_i32 s37, s37, 1
.Lt10_flag:
.LBB0_1479:
	s_add_u32 s38, s22, s34
	s_addc_u32 s39, s23, s35
	s_add_u32 s38, s38, 0x100
	s_addc_u32 s39, s39, 0
	s_add_u32 s55, s50, s34
	s_addc_u32 s56, s51, s35
	s_add_i32 s57, 0, 0x10000
	s_cmpk_eq_i32 s34, 0x300
	s_cselect_b32 s41, s19, s39
	s_cselect_b32 s40, s52, s38
	v_add_u32_e32 v114, s57, v182
	s_cselect_b32 s39, s21, s56
	s_cselect_b32 s38, s53, s55
	s_add_i32 s55, 0, 0x14000
	ds_read_b128 v[136:139], v114
	ds_read_b128 v[152:155], v114 offset:1024
	ds_read_b128 v[156:159], v114 offset:2048
	ds_read_b128 v[160:163], v114 offset:3072
	v_add_u32_e32 v114, s55, v182
	ds_read_b128 v[188:191], v114
	ds_read_b128 v[192:195], v114 offset:1024
	ds_read_b128 v[196:199], v114 offset:2048
	ds_read_b128 v[200:203], v114 offset:3072
	v_lshl_add_u64 v[164:165], v[132:133], 0, s[34:35]
	s_add_i32 m0, s43, 0xc000
	ds_read_b128 v[204:207], v184
	ds_read_b128 v[208:211], v184 offset:1024
	ds_read_b128 v[212:215], v184 offset:2048
	ds_read_b128 v[216:219], v184 offset:3072
	ds_read_b128 v[220:223], v184 offset:4096
	ds_read_b128 v[234:237], v184 offset:5120
	ds_read_b128 v[238:241], v184 offset:6144
	ds_read_b128 v[242:245], v184 offset:7168
	global_load_lds_dwordx4 v[164:165], off
	v_lshl_add_u64 v[164:165], v[134:135], 0, s[34:35]
	s_add_i32 m0, s43, 0xe000
	s_nop 0
	global_load_lds_dwordx4 v[164:165], off
	s_waitcnt vmcnt(8)
	s_waitcnt lgkmcnt(0)
	s_barrier
	s_bitcmp1_b32 s37, 0
	s_cbranch_scc1 .Lt10_k0
	s_setprio 1
	s_waitcnt lgkmcnt(0)
	v_mfma_f32_16x16x32_bf16 v[6:9], v[136:139], v[204:207], v[6:9]
	v_mfma_f32_16x16x32_bf16 v[128:131], v[156:159], v[204:207], v[128:131]
	v_mfma_f32_16x16x32_bf16 v[124:127], v[136:139], v[212:215], v[124:127]
	v_mfma_f32_16x16x32_bf16 v[120:123], v[156:159], v[212:215], v[120:123]
	v_mfma_f32_16x16x32_bf16 v[116:119], v[136:139], v[220:223], v[116:119]
	v_mfma_f32_16x16x32_bf16 v[110:113], v[156:159], v[220:223], v[110:113]
	v_mfma_f32_16x16x32_bf16 v[106:109], v[136:139], v[238:241], v[106:109]
	v_mfma_f32_16x16x32_bf16 v[102:105], v[156:159], v[238:241], v[102:105]
	v_mfma_f32_16x16x32_bf16 v[6:9], v[152:155], v[208:211], v[6:9]
	v_mfma_f32_16x16x32_bf16 v[128:131], v[160:163], v[208:211], v[128:131]
	v_mfma_f32_16x16x32_bf16 v[124:127], v[152:155], v[216:219], v[124:127]
	v_mfma_f32_16x16x32_bf16 v[120:123], v[160:163], v[216:219], v[120:123]
	v_mfma_f32_16x16x32_bf16 v[116:119], v[152:155], v[234:237], v[116:119]
	v_mfma_f32_16x16x32_bf16 v[110:113], v[160:163], v[234:237], v[110:113]
	v_mfma_f32_16x16x32_bf16 v[106:109], v[152:155], v[242:245], v[106:109]
	v_mfma_f32_16x16x32_bf16 v[102:105], v[160:163], v[242:245], v[102:105]
	s_setprio 0
	s_setprio 1
	v_mfma_f32_16x16x32_bf16 v[98:101], v[188:191], v[204:207], v[98:101]
	v_mfma_f32_16x16x32_bf16 v[94:97], v[196:199], v[204:207], v[94:97]
	v_mfma_f32_16x16x32_bf16 v[90:93], v[188:191], v[212:215], v[90:93]
	v_mfma_f32_16x16x32_bf16 v[86:89], v[196:199], v[212:215], v[86:89]
	v_mfma_f32_16x16x32_bf16 v[82:85], v[188:191], v[220:223], v[82:85]
	v_mfma_f32_16x16x32_bf16 v[78:81], v[196:199], v[220:223], v[78:81]
	v_mfma_f32_16x16x32_bf16 v[74:77], v[188:191], v[238:241], v[74:77]
	v_mfma_f32_16x16x32_bf16 v[70:73], v[196:199], v[238:241], v[70:73]
	v_mfma_f32_16x16x32_bf16 v[98:101], v[192:195], v[208:211], v[98:101]
	v_mfma_f32_16x16x32_bf16 v[94:97], v[200:203], v[208:211], v[94:97]
	v_mfma_f32_16x16x32_bf16 v[90:93], v[192:195], v[216:219], v[90:93]
	v_mfma_f32_16x16x32_bf16 v[86:89], v[200:203], v[216:219], v[86:89]
	v_mfma_f32_16x16x32_bf16 v[82:85], v[192:195], v[234:237], v[82:85]
	v_mfma_f32_16x16x32_bf16 v[78:81], v[200:203], v[234:237], v[78:81]
	v_mfma_f32_16x16x32_bf16 v[74:77], v[192:195], v[242:245], v[74:77]
	v_mfma_f32_16x16x32_bf16 v[70:73], v[200:203], v[242:245], v[70:73]
	s_setprio 0
.Lt10_k0:
	s_barrier
	s_add_i32 s56, s57, s42
	v_lshl_add_u64 v[164:165], s[38:39], 0, v[142:143]
	s_mov_b32 m0, s56
	ds_read_b128 v[204:207], v184 offset:16384
	ds_read_b128 v[208:211], v184 offset:17408
	ds_read_b128 v[212:215], v184 offset:18432
	ds_read_b128 v[216:219], v184 offset:19456
	ds_read_b128 v[220:223], v184 offset:20480
	ds_read_b128 v[234:237], v184 offset:21504
	ds_read_b128 v[238:241], v184 offset:22528
	ds_read_b128 v[242:245], v184 offset:23552
	global_load_lds_dwordx4 v[164:165], off
	s_add_i32 m0, s56, 0x2000
	s_add_u32 s56, s38, 0x20000
	v_lshl_add_u64 v[246:247], s[38:39], 0, v[146:147]
	s_addc_u32 s57, s39, 0
	s_add_i32 s55, s55, s42
	global_load_lds_dwordx4 v[246:247], off
	v_lshl_add_u64 v[248:249], s[56:57], 0, v[142:143]
	s_mov_b32 m0, s55
	v_lshl_add_u64 v[230:231], s[40:41], 0, v[144:145]
	global_load_lds_dwordx4 v[248:249], off
	v_lshl_add_u64 v[248:249], s[56:57], 0, v[146:147]
	s_add_i32 m0, s55, 0x2000
	s_nop 0
	global_load_lds_dwordx4 v[248:249], off
	v_lshl_add_u64 v[248:249], s[40:41], 0, v[140:141]
	s_mov_b32 m0, s43
	s_nop 0
	global_load_lds_dwordx4 v[248:249], off
	s_mov_b32 m0, s44
	s_nop 0
	global_load_lds_dwordx4 v[230:231], off
	s_waitcnt vmcnt(8)
	s_waitcnt lgkmcnt(0)
	s_barrier
	s_bitcmp1_b32 s37, 1
	s_cbranch_scc1 .Lt10_k1
	s_setprio 1
	s_waitcnt lgkmcnt(0)
	v_mfma_f32_16x16x32_bf16 v[66:69], v[136:139], v[204:207], v[66:69]
	v_mfma_f32_16x16x32_bf16 v[62:65], v[156:159], v[204:207], v[62:65]
	v_mfma_f32_16x16x32_bf16 v[58:61], v[136:139], v[212:215], v[58:61]
	v_mfma_f32_16x16x32_bf16 v[54:57], v[156:159], v[212:215], v[54:57]
	v_mfma_f32_16x16x32_bf16 v[50:53], v[136:139], v[220:223], v[50:53]
	v_mfma_f32_16x16x32_bf16 v[46:49], v[156:159], v[220:223], v[46:49]
	v_mfma_f32_16x16x32_bf16 v[42:45], v[136:139], v[238:241], v[42:45]
	v_mfma_f32_16x16x32_bf16 v[38:41], v[156:159], v[238:241], v[38:41]
	v_mfma_f32_16x16x32_bf16 v[66:69], v[152:155], v[208:211], v[66:69]
	v_mfma_f32_16x16x32_bf16 v[62:65], v[160:163], v[208:211], v[62:65]
	v_mfma_f32_16x16x32_bf16 v[58:61], v[152:155], v[216:219], v[58:61]
	v_mfma_f32_16x16x32_bf16 v[54:57], v[160:163], v[216:219], v[54:57]
	v_mfma_f32_16x16x32_bf16 v[50:53], v[152:155], v[234:237], v[50:53]
	v_mfma_f32_16x16x32_bf16 v[46:49], v[160:163], v[234:237], v[46:49]
	v_mfma_f32_16x16x32_bf16 v[42:45], v[152:155], v[242:245], v[42:45]
	v_mfma_f32_16x16x32_bf16 v[38:41], v[160:163], v[242:245], v[38:41]
	s_setprio 0
	s_setprio 1
	v_mfma_f32_16x16x32_bf16 v[34:37], v[188:191], v[204:207], v[34:37]
	v_mfma_f32_16x16x32_bf16 v[30:33], v[196:199], v[204:207], v[30:33]
	v_mfma_f32_16x16x32_bf16 v[26:29], v[188:191], v[212:215], v[26:29]
	v_mfma_f32_16x16x32_bf16 v[22:25], v[196:199], v[212:215], v[22:25]
	v_mfma_f32_16x16x32_bf16 v[18:21], v[188:191], v[220:223], v[18:21]
	v_mfma_f32_16x16x32_bf16 v[14:17], v[196:199], v[220:223], v[14:17]
	v_mfma_f32_16x16x32_bf16 v[10:13], v[188:191], v[238:241], v[10:13]
	v_mfma_f32_16x16x32_bf16 v[2:5], v[196:199], v[238:241], v[2:5]
	v_mfma_f32_16x16x32_bf16 v[34:37], v[192:195], v[208:211], v[34:37]
	v_mfma_f32_16x16x32_bf16 v[30:33], v[200:203], v[208:211], v[30:33]
	v_mfma_f32_16x16x32_bf16 v[26:29], v[192:195], v[216:219], v[26:29]
	v_mfma_f32_16x16x32_bf16 v[22:25], v[200:203], v[216:219], v[22:25]
	v_mfma_f32_16x16x32_bf16 v[18:21], v[192:195], v[234:237], v[18:21]
	v_mfma_f32_16x16x32_bf16 v[14:17], v[200:203], v[234:237], v[14:17]
	v_mfma_f32_16x16x32_bf16 v[10:13], v[192:195], v[242:245], v[10:13]
	v_mfma_f32_16x16x32_bf16 v[2:5], v[200:203], v[242:245], v[2:5]
	s_setprio 0
.Lt10_k1:
	s_barrier
	s_add_i32 s55, 0, 0x18000
	v_add_u32_e32 v114, s55, v182
	s_add_i32 s56, 0, 0x1c000
	ds_read_b128 v[136:139], v114
	ds_read_b128 v[152:155], v114 offset:1024
	ds_read_b128 v[156:159], v114 offset:2048
	ds_read_b128 v[160:163], v114 offset:3072
	v_add_u32_e32 v114, s56, v182
	ds_read_b128 v[188:191], v114
	ds_read_b128 v[192:195], v114 offset:1024
	ds_read_b128 v[196:199], v114 offset:2048
	ds_read_b128 v[200:203], v114 offset:3072
	s_add_u32 s40, s40, 0x20000
	s_addc_u32 s41, s41, 0
	s_mov_b32 m0, s45
	v_lshl_add_u64 v[168:169], s[40:41], 0, v[140:141]
	ds_read_b128 v[204:207], v184 offset:32768
	ds_read_b128 v[208:211], v184 offset:33792
	ds_read_b128 v[212:215], v184 offset:34816
	ds_read_b128 v[216:219], v184 offset:35840
	ds_read_b128 v[220:223], v184 offset:36864
	ds_read_b128 v[234:237], v184 offset:37888
	ds_read_b128 v[238:241], v184 offset:38912
	ds_read_b128 v[242:245], v184 offset:39936
	global_load_lds_dwordx4 v[168:169], off
	v_lshl_add_u64 v[168:169], s[40:41], 0, v[144:145]
	s_mov_b32 m0, s46
	s_nop 0
	global_load_lds_dwordx4 v[168:169], off
	s_waitcnt vmcnt(8)
	s_waitcnt lgkmcnt(0)
	s_barrier
	s_bitcmp1_b32 s37, 0
	s_cbranch_scc1 .Lt10_k2
	s_setprio 1
	s_waitcnt lgkmcnt(0)
	v_mfma_f32_16x16x32_bf16 v[6:9], v[136:139], v[204:207], v[6:9]
	v_mfma_f32_16x16x32_bf16 v[128:131], v[156:159], v[204:207], v[128:131]
	v_mfma_f32_16x16x32_bf16 v[124:127], v[136:139], v[212:215], v[124:127]
	v_mfma_f32_16x16x32_bf16 v[120:123], v[156:159], v[212:215], v[120:123]
	v_mfma_f32_16x16x32_bf16 v[116:119], v[136:139], v[220:223], v[116:119]
	v_mfma_f32_16x16x32_bf16 v[110:113], v[156:159], v[220:223], v[110:113]
	v_mfma_f32_16x16x32_bf16 v[106:109], v[136:139], v[238:241], v[106:109]
	v_mfma_f32_16x16x32_bf16 v[102:105], v[156:159], v[238:241], v[102:105]
	v_mfma_f32_16x16x32_bf16 v[6:9], v[152:155], v[208:211], v[6:9]
	v_mfma_f32_16x16x32_bf16 v[128:131], v[160:163], v[208:211], v[128:131]
	v_mfma_f32_16x16x32_bf16 v[124:127], v[152:155], v[216:219], v[124:127]
	v_mfma_f32_16x16x32_bf16 v[120:123], v[160:163], v[216:219], v[120:123]
	v_mfma_f32_16x16x32_bf16 v[116:119], v[152:155], v[234:237], v[116:119]
	v_mfma_f32_16x16x32_bf16 v[110:113], v[160:163], v[234:237], v[110:113]
	v_mfma_f32_16x16x32_bf16 v[106:109], v[152:155], v[242:245], v[106:109]
	v_mfma_f32_16x16x32_bf16 v[102:105], v[160:163], v[242:245], v[102:105]
	s_setprio 0
	s_setprio 1
	v_mfma_f32_16x16x32_bf16 v[98:101], v[188:191], v[204:207], v[98:101]
	v_mfma_f32_16x16x32_bf16 v[94:97], v[196:199], v[204:207], v[94:97]
	v_mfma_f32_16x16x32_bf16 v[90:93], v[188:191], v[212:215], v[90:93]
	v_mfma_f32_16x16x32_bf16 v[86:89], v[196:199], v[212:215], v[86:89]
	v_mfma_f32_16x16x32_bf16 v[82:85], v[188:191], v[220:223], v[82:85]
	v_mfma_f32_16x16x32_bf16 v[78:81], v[196:199], v[220:223], v[78:81]
	v_mfma_f32_16x16x32_bf16 v[74:77], v[188:191], v[238:241], v[74:77]
	v_mfma_f32_16x16x32_bf16 v[70:73], v[196:199], v[238:241], v[70:73]
	v_mfma_f32_16x16x32_bf16 v[98:101], v[192:195], v[208:211], v[98:101]
	v_mfma_f32_16x16x32_bf16 v[94:97], v[200:203], v[208:211], v[94:97]
	v_mfma_f32_16x16x32_bf16 v[90:93], v[192:195], v[216:219], v[90:93]
	v_mfma_f32_16x16x32_bf16 v[86:89], v[200:203], v[216:219], v[86:89]
	v_mfma_f32_16x16x32_bf16 v[82:85], v[192:195], v[234:237], v[82:85]
	v_mfma_f32_16x16x32_bf16 v[78:81], v[200:203], v[234:237], v[78:81]
	v_mfma_f32_16x16x32_bf16 v[74:77], v[192:195], v[242:245], v[74:77]
	v_mfma_f32_16x16x32_bf16 v[70:73], v[200:203], v[242:245], v[70:73]
	s_setprio 0
.Lt10_k2:
	s_barrier
	s_add_i32 s40, s55, s42
	v_lshl_add_u64 v[164:165], v[164:165], 0, s[78:79]
	s_mov_b32 m0, s40
	ds_read_b128 v[204:207], v184 offset:49152
	ds_read_b128 v[208:211], v184 offset:50176
	ds_read_b128 v[212:215], v184 offset:51200
	ds_read_b128 v[216:219], v184 offset:52224
	ds_read_b128 v[220:223], v184 offset:53248
	ds_read_b128 v[234:237], v184 offset:54272
	ds_read_b128 v[238:241], v184 offset:55296
	ds_read_b128 v[242:245], v184 offset:56320
	global_load_lds_dwordx4 v[164:165], off
	s_add_i32 m0, s40, 0x2000
	s_add_u32 s38, s38, 0x20080
	v_lshl_add_u64 v[164:165], v[246:247], 0, s[78:79]
	s_addc_u32 s39, s39, 0
	s_add_i32 s40, s56, s42
	global_load_lds_dwordx4 v[164:165], off
	v_lshl_add_u64 v[164:165], s[38:39], 0, v[142:143]
	s_mov_b32 m0, s40
	s_nop 0
	global_load_lds_dwordx4 v[164:165], off
	v_lshl_add_u64 v[164:165], s[38:39], 0, v[146:147]
	s_add_i32 m0, s40, 0x2000
	s_nop 0
	global_load_lds_dwordx4 v[164:165], off
	v_lshl_add_u64 v[164:165], v[248:249], 0, s[78:79]
	s_mov_b32 m0, s47
	s_nop 0
	global_load_lds_dwordx4 v[164:165], off
	v_lshl_add_u64 v[164:165], v[230:231], 0, s[78:79]
	s_mov_b32 m0, s48
	s_nop 0
	global_load_lds_dwordx4 v[164:165], off
	s_waitcnt vmcnt(8)
	s_waitcnt lgkmcnt(0)
	s_barrier
	s_bitcmp1_b32 s37, 1
	s_cbranch_scc1 .Lt10_k3
	s_setprio 1
	s_waitcnt lgkmcnt(0)
	v_mfma_f32_16x16x32_bf16 v[66:69], v[136:139], v[204:207], v[66:69]
	v_mfma_f32_16x16x32_bf16 v[62:65], v[156:159], v[204:207], v[62:65]
	v_mfma_f32_16x16x32_bf16 v[58:61], v[136:139], v[212:215], v[58:61]
	v_mfma_f32_16x16x32_bf16 v[54:57], v[156:159], v[212:215], v[54:57]
	v_mfma_f32_16x16x32_bf16 v[50:53], v[136:139], v[220:223], v[50:53]
	v_mfma_f32_16x16x32_bf16 v[46:49], v[156:159], v[220:223], v[46:49]
	v_mfma_f32_16x16x32_bf16 v[42:45], v[136:139], v[238:241], v[42:45]
	v_mfma_f32_16x16x32_bf16 v[38:41], v[156:159], v[238:241], v[38:41]
	v_mfma_f32_16x16x32_bf16 v[66:69], v[152:155], v[208:211], v[66:69]
	v_mfma_f32_16x16x32_bf16 v[62:65], v[160:163], v[208:211], v[62:65]
	v_mfma_f32_16x16x32_bf16 v[58:61], v[152:155], v[216:219], v[58:61]
	v_mfma_f32_16x16x32_bf16 v[54:57], v[160:163], v[216:219], v[54:57]
	v_mfma_f32_16x16x32_bf16 v[50:53], v[152:155], v[234:237], v[50:53]
	v_mfma_f32_16x16x32_bf16 v[46:49], v[160:163], v[234:237], v[46:49]
	v_mfma_f32_16x16x32_bf16 v[42:45], v[152:155], v[242:245], v[42:45]
	v_mfma_f32_16x16x32_bf16 v[38:41], v[160:163], v[242:245], v[38:41]
	s_setprio 0
	s_setprio 1
	v_mfma_f32_16x16x32_bf16 v[34:37], v[188:191], v[204:207], v[34:37]
	v_mfma_f32_16x16x32_bf16 v[30:33], v[196:199], v[204:207], v[30:33]
	v_mfma_f32_16x16x32_bf16 v[26:29], v[188:191], v[212:215], v[26:29]
	v_mfma_f32_16x16x32_bf16 v[22:25], v[196:199], v[212:215], v[22:25]
	v_mfma_f32_16x16x32_bf16 v[18:21], v[188:191], v[220:223], v[18:21]
	v_mfma_f32_16x16x32_bf16 v[14:17], v[196:199], v[220:223], v[14:17]
	v_mfma_f32_16x16x32_bf16 v[10:13], v[188:191], v[238:241], v[10:13]
	v_mfma_f32_16x16x32_bf16 v[2:5], v[196:199], v[238:241], v[2:5]
	v_mfma_f32_16x16x32_bf16 v[34:37], v[192:195], v[208:211], v[34:37]
	v_mfma_f32_16x16x32_bf16 v[30:33], v[200:203], v[208:211], v[30:33]
	v_mfma_f32_16x16x32_bf16 v[26:29], v[192:195], v[216:219], v[26:29]
	v_mfma_f32_16x16x32_bf16 v[22:25], v[200:203], v[216:219], v[22:25]
	v_mfma_f32_16x16x32_bf16 v[18:21], v[192:195], v[234:237], v[18:21]
	v_mfma_f32_16x16x32_bf16 v[14:17], v[200:203], v[234:237], v[14:17]
	v_mfma_f32_16x16x32_bf16 v[10:13], v[192:195], v[242:245], v[10:13]
	v_mfma_f32_16x16x32_bf16 v[2:5], v[200:203], v[242:245], v[2:5]
	s_setprio 0
.Lt10_k3:
	s_barrier
	s_add_i32 s54, s54, 2
	s_add_u32 s34, s34, 0x100
	s_addc_u32 s35, s35, 0
	s_cmp_gt_u32 s54, 5
	s_cbranch_scc0 .LBB0_1479
	s_and_b64 vcc, exec, s[16:17]
	s_cbranch_vccz .LBB0_1482
	s_barrier
.LBB0_1482:
	s_lshl_b32 s19, s0, 8
	s_and_b32 s19, s19, 0x300
	v_or_b32_e32 v187, s19, v183
	v_add_u32_e32 v152, v181, v1
	s_waitcnt vmcnt(0)
	s_bitcmp1_b32 s37, 0
	s_cbranch_scc0 .Lt10_m0
	v_mov_b32_e32 v167, -1
	v_mov_b32_e32 v166, -1
	v_mov_b32_e32 v173, -1
	v_mov_b32_e32 v172, -1
.Lt10_m0:
	s_bitcmp1_b32 s37, 1
	s_cbranch_scc0 .Lt10_m1
	v_mov_b32_e32 v178, -1
	v_mov_b32_e32 v177, -1
	v_mov_b32_e32 v180, -1
	v_mov_b32_e32 v179, -1
.Lt10_m1:
	v_and_b32_e32 v230, 0x80000001, v167
	v_cmp_eq_u32_e32 vcc, 0, v230
	s_and_saveexec_b64 s[38:39], vcc
	v_lshrrev_b32_e32 v230, 1, v167
	v_mov_b32_e32 v231, 0
	v_lshlrev_b64 v[230:231], 10, v[230:231]
	v_or_b32_e32 v230, v230, v187
	v_lshl_add_u64 v[230:231], v[230:231], 1, s[92:93]
	global_load_dwordx4 v[192:195], v[230:231], off
	global_load_dwordx4 v[196:199], v[230:231], off offset:256
	s_or_b64 exec, exec, s[38:39]
	v_and_b32_e32 v230, 0x80000001, v166
	v_cmp_eq_u32_e32 vcc, 0, v230
	s_and_saveexec_b64 s[38:39], vcc
	v_lshrrev_b32_e32 v230, 1, v166
	v_mov_b32_e32 v231, 0
	v_lshlrev_b64 v[230:231], 10, v[230:231]
	v_or_b32_e32 v230, v230, v187
	v_lshl_add_u64 v[230:231], v[230:231], 1, s[92:93]
	global_load_dwordx4 v[200:203], v[230:231], off
	global_load_dwordx4 v[204:207], v[230:231], off offset:256
	s_or_b64 exec, exec, s[38:39]
	v_and_b32_e32 v230, 0x80000001, v173
	v_cmp_eq_u32_e32 vcc, 0, v230
	s_and_saveexec_b64 s[38:39], vcc
	v_lshrrev_b32_e32 v230, 1, v173
	v_mov_b32_e32 v231, 0
	v_lshlrev_b64 v[230:231], 10, v[230:231]
	v_or_b32_e32 v230, v230, v187
	v_lshl_add_u64 v[230:231], v[230:231], 1, s[92:93]
	global_load_dwordx4 v[208:211], v[230:231], off
	global_load_dwordx4 v[212:215], v[230:231], off offset:256
	s_or_b64 exec, exec, s[38:39]
	v_and_b32_e32 v230, 0x80000001, v172
	v_cmp_eq_u32_e32 vcc, 0, v230
	s_and_saveexec_b64 s[38:39], vcc
	v_lshrrev_b32_e32 v230, 1, v172
	v_mov_b32_e32 v231, 0
	v_lshlrev_b64 v[230:231], 10, v[230:231]
	v_or_b32_e32 v230, v230, v187
	v_lshl_add_u64 v[230:231], v[230:231], 1, s[92:93]
	global_load_dwordx4 v[216:219], v[230:231], off
	global_load_dwordx4 v[220:223], v[230:231], off offset:256
	s_or_b64 exec, exec, s[38:39]
	v_and_b32_e32 v230, 0x80000001, v178
	v_cmp_eq_u32_e32 vcc, 0, v230
	s_and_saveexec_b64 s[38:39], vcc
	v_lshrrev_b32_e32 v230, 1, v178
	v_mov_b32_e32 v231, 0
	v_lshlrev_b64 v[230:231], 10, v[230:231]
	v_or_b32_e32 v230, v230, v187
	v_lshl_add_u64 v[230:231], v[230:231], 1, s[92:93]
	global_load_dwordx4 v[234:237], v[230:231], off
	global_load_dwordx4 v[238:241], v[230:231], off offset:256
	s_or_b64 exec, exec, s[38:39]
	v_and_b32_e32 v230, 0x80000001, v177
	v_cmp_eq_u32_e32 vcc, 0, v230
	s_and_saveexec_b64 s[38:39], vcc
	v_lshrrev_b32_e32 v230, 1, v177
	v_mov_b32_e32 v231, 0
	v_lshlrev_b64 v[230:231], 10, v[230:231]
	v_or_b32_e32 v230, v230, v187
	v_lshl_add_u64 v[230:231], v[230:231], 1, s[92:93]
	global_load_dwordx4 v[242:245], v[230:231], off
	global_load_dwordx4 v[246:249], v[230:231], off offset:256
	s_or_b64 exec, exec, s[38:39]
	v_cmp_lt_i32_e32 vcc, -1, v167
	v_ashrrev_i32_e32 v153, 31, v152
	v_lshlrev_b32_e32 v154, 2, v187
	v_add_u32_e32 v154, 0x21000, v154
	v_readlane_b32 s36, v253, 38
	v_readlane_b32 s37, v253, 39
	s_nop 1
	v_lshl_add_u64 v[156:157], v[152:153], 2, s[36:37]
	global_load_dword v158, v[156:157], off
	global_load_dword v189, v[156:157], off offset:64
	global_load_dword v190, v[156:157], off offset:128
	global_load_dword v191, v[156:157], off offset:192
	global_load_dword v250, v[156:157], off offset:640
	global_load_dword v155, v[156:157], off offset:704
	global_load_dword v152, v[156:157], off offset:512
	global_load_dword v153, v[156:157], off offset:576
	s_waitcnt vmcnt(0)
	s_and_saveexec_b64 s[34:35], vcc
	s_cbranch_execz .LBB0_1491
	v_lshrrev_b32_e32 v114, 14, v167
	v_lshl_add_u32 v160, v114, 12, v154
	ds_read_b128 v[132:135], v160
	ds_read_b128 v[136:139], v160 offset:16
	v_lshrrev_b32_e32 v156, 1, v167
	v_mov_b32_e32 v157, v115
	v_and_b32_e32 v114, 1, v167
	v_lshlrev_b64 v[156:157], 10, v[156:157]
	v_cmp_eq_u32_e32 vcc, 1, v114
	v_or_b32_e32 v162, v156, v187
	v_mov_b32_e32 v163, v157
	s_waitcnt lgkmcnt(1)
	v_pk_mul_f32 v[134:135], v[8:9], v[134:135]
	v_pk_mul_f32 v[132:133], v[6:7], v[132:133]
	s_waitcnt lgkmcnt(0)
	v_pk_mul_f32 v[138:139], v[130:131], v[138:139]
	v_pk_mul_f32 v[168:169], v[128:129], v[136:137]
	v_pk_mul_f32 v[164:165], v[158:159], v[134:135] op_sel_hi:[0,1]
	v_pk_mul_f32 v[136:137], v[158:159], v[132:133] op_sel_hi:[0,1]
	v_pk_mul_f32 v[138:139], v[158:159], v[138:139] op_sel_hi:[0,1]
	v_pk_mul_f32 v[132:133], v[158:159], v[168:169] op_sel_hi:[0,1]
	s_and_saveexec_b64 s[38:39], vcc
	s_xor_b64 s[38:39], exec, s[38:39]
	s_cbranch_execz .LBB0_1485
	v_cvt_pk_bf16_f32 v134, v136, v137
	v_cvt_pk_bf16_f32 v135, v164, v165
	v_cvt_pk_bf16_f32 v136, v132, v133
	v_cvt_pk_bf16_f32 v137, v138, v139
	v_lshl_add_u64 v[132:133], v[162:163], 1, s[4:5]
	global_store_dwordx4 v[132:133], v[134:137], off
